# speedup vs baseline: 1.0200x; 1.0192x over previous
_Z11prep_kernelPKfS0_S0_PDF16_PfPiS0_S1_:
	s_cmpk_lt_u32 s2, 0xc1
	s_mov_b64 s[4:5], -1
	s_cbranch_scc0 .LBB0_51
	s_cmpk_lg_i32 s2, 0xc0
	s_cbranch_scc0 .LBB0_11
	s_cmp_gt_u32 s2, 63
	s_cbranch_scc0 .LBB0_8
	s_load_dwordx4 s[4:7], s[0:1], 0x0
	s_load_dwordx2 s[28:29], s[0:1], 0x20
	s_sub_u32 s3, s2, 64
	v_readfirstlane_b32 s23, v0
	v_and_b32_e32 v1, 63, v0
	v_lshlrev_b32_e32 v26, 4, v1
	v_mov_b32_e32 v27, 0
	s_lshr_b32 s23, s23, 6
	s_and_b32 s22, s23, 3
	s_lshr_b32 s26, s23, 2
	s_lshr_b32 s27, s3, 1
	s_and_b32 s30, s3, 1
	s_lshl_b32 s8, s27, 3
	s_lshl_b32 s9, s26, 2
	s_add_u32 s31, s8, s9
	s_lshl_b32 s8, s31, 9
	s_lshl_b32 s9, s22, 7
	s_add_u32 s8, s8, s9
	s_lshl_b32 s10, s22, 16
	s_lshl_b32 s9, s30, 10
	s_add_u32 s10, s10, s9
	s_waitcnt lgkmcnt(0)
	s_add_u32 s20, s4, s8
	s_addc_u32 s21, s5, 0
	s_add_u32 s24, s6, s10
	s_addc_u32 s25, s7, 0
	global_load_dwordx4 v[32:35], v26, s[24:25]
	global_load_dwordx4 v[36:39], v26, s[24:25] offset:2048
	s_add_u32 s24, s24, 0x1000
	s_addc_u32 s25, s25, 0
	s_load_dwordx8 s[32:39], s[20:21], 0x0
	s_load_dwordx8 s[40:47], s[20:21], 0x200
	s_load_dwordx8 s[48:55], s[20:21], 0x400
	s_load_dwordx8 s[56:63], s[20:21], 0x600
	global_load_dwordx4 v[40:43], v26, s[24:25]
	global_load_dwordx4 v[44:47], v26, s[24:25] offset:2048
	s_add_u32 s24, s24, 0x1000
	s_addc_u32 s25, s25, 0
	s_load_dwordx8 s[64:71], s[20:21], 0x20
	s_load_dwordx8 s[72:79], s[20:21], 0x220
	s_load_dwordx8 s[80:87], s[20:21], 0x420
	s_load_dwordx8 s[88:95], s[20:21], 0x620
	global_load_dwordx4 v[48:51], v26, s[24:25]
	global_load_dwordx4 v[52:55], v26, s[24:25] offset:2048
	s_add_u32 s24, s24, 0x1000
	s_addc_u32 s25, s25, 0
	global_load_dwordx4 v[56:59], v26, s[24:25]
	global_load_dwordx4 v[60:63], v26, s[24:25] offset:2048
	s_add_u32 s24, s24, 0x1000
	s_addc_u32 s25, s25, 0
	global_load_dwordx4 v[64:67], v26, s[24:25]
	global_load_dwordx4 v[68:71], v26, s[24:25] offset:2048
	s_add_u32 s24, s24, 0x1000
	s_addc_u32 s25, s25, 0
	global_load_dwordx4 v[72:75], v26, s[24:25]
	global_load_dwordx4 v[76:79], v26, s[24:25] offset:2048
	s_add_u32 s24, s24, 0x1000
	s_addc_u32 s25, s25, 0
	global_load_dwordx4 v[80:83], v26, s[24:25]
	global_load_dwordx4 v[84:87], v26, s[24:25] offset:2048
	s_add_u32 s24, s24, 0x1000
	s_addc_u32 s25, s25, 0
	global_load_dwordx4 v[88:91], v26, s[24:25]
	global_load_dwordx4 v[92:95], v26, s[24:25] offset:2048
	s_add_u32 s24, s24, 0x1000
	s_addc_u32 s25, s25, 0
	global_load_dwordx4 v[96:99], v26, s[24:25]
	global_load_dwordx4 v[100:103], v26, s[24:25] offset:2048
	s_add_u32 s24, s24, 0x1000
	s_addc_u32 s25, s25, 0
	global_load_dwordx4 v[104:107], v26, s[24:25]
	global_load_dwordx4 v[108:111], v26, s[24:25] offset:2048
	s_add_u32 s24, s24, 0x1000
	s_addc_u32 s25, s25, 0
	global_load_dwordx4 v[112:115], v26, s[24:25]
	global_load_dwordx4 v[116:119], v26, s[24:25] offset:2048
	s_add_u32 s24, s24, 0x1000
	s_addc_u32 s25, s25, 0
	global_load_dwordx4 v[120:123], v26, s[24:25]
	global_load_dwordx4 v[124:127], v26, s[24:25] offset:2048
	s_add_u32 s24, s24, 0x1000
	s_addc_u32 s25, s25, 0
	global_load_dwordx4 v[128:131], v26, s[24:25]
	global_load_dwordx4 v[132:135], v26, s[24:25] offset:2048
	s_add_u32 s24, s24, 0x1000
	s_addc_u32 s25, s25, 0
	global_load_dwordx4 v[136:139], v26, s[24:25]
	global_load_dwordx4 v[140:143], v26, s[24:25] offset:2048
	s_add_u32 s24, s24, 0x1000
	s_addc_u32 s25, s25, 0
	global_load_dwordx4 v[144:147], v26, s[24:25]
	global_load_dwordx4 v[148:151], v26, s[24:25] offset:2048
	s_add_u32 s24, s24, 0x1000
	s_addc_u32 s25, s25, 0
	global_load_dwordx4 v[152:155], v26, s[24:25]
	global_load_dwordx4 v[156:159], v26, s[24:25] offset:2048
	v_mov_b64_e32 v[14:15], 0
	v_mov_b64_e32 v[16:17], 0
	v_mov_b64_e32 v[10:11], 0
	v_mov_b64_e32 v[12:13], 0
	v_mov_b64_e32 v[6:7], 0
	v_mov_b64_e32 v[8:9], 0
	v_mov_b64_e32 v[2:3], 0
	v_mov_b64_e32 v[4:5], 0
	s_waitcnt lgkmcnt(0)
	s_waitcnt vmcnt(31)
	v_pk_fma_f32 v[14:15], s[32:33], v[32:33], v[14:15] op_sel_hi:[0,1,1]
	v_pk_fma_f32 v[16:17], s[32:33], v[34:35], v[16:17] op_sel_hi:[0,1,1]
	v_pk_fma_f32 v[10:11], s[40:41], v[32:33], v[10:11] op_sel_hi:[0,1,1]
	v_pk_fma_f32 v[12:13], s[40:41], v[34:35], v[12:13] op_sel_hi:[0,1,1]
	v_pk_fma_f32 v[6:7], s[48:49], v[32:33], v[6:7] op_sel_hi:[0,1,1]
	v_pk_fma_f32 v[8:9], s[48:49], v[34:35], v[8:9] op_sel_hi:[0,1,1]
	v_pk_fma_f32 v[2:3], s[56:57], v[32:33], v[2:3] op_sel_hi:[0,1,1]
	v_pk_fma_f32 v[4:5], s[56:57], v[34:35], v[4:5] op_sel_hi:[0,1,1]
	s_waitcnt vmcnt(30)
	v_pk_fma_f32 v[14:15], s[32:33], v[36:37], v[14:15] op_sel:[1,0,0]
	v_pk_fma_f32 v[16:17], s[32:33], v[38:39], v[16:17] op_sel:[1,0,0]
	v_pk_fma_f32 v[10:11], s[40:41], v[36:37], v[10:11] op_sel:[1,0,0]
	v_pk_fma_f32 v[12:13], s[40:41], v[38:39], v[12:13] op_sel:[1,0,0]
	v_pk_fma_f32 v[6:7], s[48:49], v[36:37], v[6:7] op_sel:[1,0,0]
	v_pk_fma_f32 v[8:9], s[48:49], v[38:39], v[8:9] op_sel:[1,0,0]
	v_pk_fma_f32 v[2:3], s[56:57], v[36:37], v[2:3] op_sel:[1,0,0]
	v_pk_fma_f32 v[4:5], s[56:57], v[38:39], v[4:5] op_sel:[1,0,0]
	s_waitcnt vmcnt(29)
	v_pk_fma_f32 v[14:15], s[34:35], v[40:41], v[14:15] op_sel_hi:[0,1,1]
	v_pk_fma_f32 v[16:17], s[34:35], v[42:43], v[16:17] op_sel_hi:[0,1,1]
	v_pk_fma_f32 v[10:11], s[42:43], v[40:41], v[10:11] op_sel_hi:[0,1,1]
	v_pk_fma_f32 v[12:13], s[42:43], v[42:43], v[12:13] op_sel_hi:[0,1,1]
	v_pk_fma_f32 v[6:7], s[50:51], v[40:41], v[6:7] op_sel_hi:[0,1,1]
	v_pk_fma_f32 v[8:9], s[50:51], v[42:43], v[8:9] op_sel_hi:[0,1,1]
	v_pk_fma_f32 v[2:3], s[58:59], v[40:41], v[2:3] op_sel_hi:[0,1,1]
	v_pk_fma_f32 v[4:5], s[58:59], v[42:43], v[4:5] op_sel_hi:[0,1,1]
	s_waitcnt vmcnt(28)
	v_pk_fma_f32 v[14:15], s[34:35], v[44:45], v[14:15] op_sel:[1,0,0]
	v_pk_fma_f32 v[16:17], s[34:35], v[46:47], v[16:17] op_sel:[1,0,0]
	v_pk_fma_f32 v[10:11], s[42:43], v[44:45], v[10:11] op_sel:[1,0,0]
	v_pk_fma_f32 v[12:13], s[42:43], v[46:47], v[12:13] op_sel:[1,0,0]
	v_pk_fma_f32 v[6:7], s[50:51], v[44:45], v[6:7] op_sel:[1,0,0]
	v_pk_fma_f32 v[8:9], s[50:51], v[46:47], v[8:9] op_sel:[1,0,0]
	v_pk_fma_f32 v[2:3], s[58:59], v[44:45], v[2:3] op_sel:[1,0,0]
	v_pk_fma_f32 v[4:5], s[58:59], v[46:47], v[4:5] op_sel:[1,0,0]
	s_waitcnt vmcnt(27)
	v_pk_fma_f32 v[14:15], s[36:37], v[48:49], v[14:15] op_sel_hi:[0,1,1]
	v_pk_fma_f32 v[16:17], s[36:37], v[50:51], v[16:17] op_sel_hi:[0,1,1]
	v_pk_fma_f32 v[10:11], s[44:45], v[48:49], v[10:11] op_sel_hi:[0,1,1]
	v_pk_fma_f32 v[12:13], s[44:45], v[50:51], v[12:13] op_sel_hi:[0,1,1]
	v_pk_fma_f32 v[6:7], s[52:53], v[48:49], v[6:7] op_sel_hi:[0,1,1]
	v_pk_fma_f32 v[8:9], s[52:53], v[50:51], v[8:9] op_sel_hi:[0,1,1]
	v_pk_fma_f32 v[2:3], s[60:61], v[48:49], v[2:3] op_sel_hi:[0,1,1]
	v_pk_fma_f32 v[4:5], s[60:61], v[50:51], v[4:5] op_sel_hi:[0,1,1]
	s_waitcnt vmcnt(26)
	v_pk_fma_f32 v[14:15], s[36:37], v[52:53], v[14:15] op_sel:[1,0,0]
	v_pk_fma_f32 v[16:17], s[36:37], v[54:55], v[16:17] op_sel:[1,0,0]
	v_pk_fma_f32 v[10:11], s[44:45], v[52:53], v[10:11] op_sel:[1,0,0]
	v_pk_fma_f32 v[12:13], s[44:45], v[54:55], v[12:13] op_sel:[1,0,0]
	v_pk_fma_f32 v[6:7], s[52:53], v[52:53], v[6:7] op_sel:[1,0,0]
	v_pk_fma_f32 v[8:9], s[52:53], v[54:55], v[8:9] op_sel:[1,0,0]
	v_pk_fma_f32 v[2:3], s[60:61], v[52:53], v[2:3] op_sel:[1,0,0]
	v_pk_fma_f32 v[4:5], s[60:61], v[54:55], v[4:5] op_sel:[1,0,0]
	s_waitcnt vmcnt(25)
	v_pk_fma_f32 v[14:15], s[38:39], v[56:57], v[14:15] op_sel_hi:[0,1,1]
	v_pk_fma_f32 v[16:17], s[38:39], v[58:59], v[16:17] op_sel_hi:[0,1,1]
	v_pk_fma_f32 v[10:11], s[46:47], v[56:57], v[10:11] op_sel_hi:[0,1,1]
	v_pk_fma_f32 v[12:13], s[46:47], v[58:59], v[12:13] op_sel_hi:[0,1,1]
	v_pk_fma_f32 v[6:7], s[54:55], v[56:57], v[6:7] op_sel_hi:[0,1,1]
	v_pk_fma_f32 v[8:9], s[54:55], v[58:59], v[8:9] op_sel_hi:[0,1,1]
	v_pk_fma_f32 v[2:3], s[62:63], v[56:57], v[2:3] op_sel_hi:[0,1,1]
	v_pk_fma_f32 v[4:5], s[62:63], v[58:59], v[4:5] op_sel_hi:[0,1,1]
	s_waitcnt vmcnt(24)
	v_pk_fma_f32 v[14:15], s[38:39], v[60:61], v[14:15] op_sel:[1,0,0]
	v_pk_fma_f32 v[16:17], s[38:39], v[62:63], v[16:17] op_sel:[1,0,0]
	v_pk_fma_f32 v[10:11], s[46:47], v[60:61], v[10:11] op_sel:[1,0,0]
	v_pk_fma_f32 v[12:13], s[46:47], v[62:63], v[12:13] op_sel:[1,0,0]
	v_pk_fma_f32 v[6:7], s[54:55], v[60:61], v[6:7] op_sel:[1,0,0]
	v_pk_fma_f32 v[8:9], s[54:55], v[62:63], v[8:9] op_sel:[1,0,0]
	v_pk_fma_f32 v[2:3], s[62:63], v[60:61], v[2:3] op_sel:[1,0,0]
	v_pk_fma_f32 v[4:5], s[62:63], v[62:63], v[4:5] op_sel:[1,0,0]
	s_load_dwordx8 s[32:39], s[20:21], 0x40
	s_load_dwordx8 s[40:47], s[20:21], 0x240
	s_load_dwordx8 s[48:55], s[20:21], 0x440
	s_load_dwordx8 s[56:63], s[20:21], 0x640
	s_waitcnt vmcnt(23)
	v_pk_fma_f32 v[14:15], s[64:65], v[64:65], v[14:15] op_sel_hi:[0,1,1]
	v_pk_fma_f32 v[16:17], s[64:65], v[66:67], v[16:17] op_sel_hi:[0,1,1]
	v_pk_fma_f32 v[10:11], s[72:73], v[64:65], v[10:11] op_sel_hi:[0,1,1]
	v_pk_fma_f32 v[12:13], s[72:73], v[66:67], v[12:13] op_sel_hi:[0,1,1]
	v_pk_fma_f32 v[6:7], s[80:81], v[64:65], v[6:7] op_sel_hi:[0,1,1]
	v_pk_fma_f32 v[8:9], s[80:81], v[66:67], v[8:9] op_sel_hi:[0,1,1]
	v_pk_fma_f32 v[2:3], s[88:89], v[64:65], v[2:3] op_sel_hi:[0,1,1]
	v_pk_fma_f32 v[4:5], s[88:89], v[66:67], v[4:5] op_sel_hi:[0,1,1]
	s_waitcnt vmcnt(22)
	v_pk_fma_f32 v[14:15], s[64:65], v[68:69], v[14:15] op_sel:[1,0,0]
	v_pk_fma_f32 v[16:17], s[64:65], v[70:71], v[16:17] op_sel:[1,0,0]
	v_pk_fma_f32 v[10:11], s[72:73], v[68:69], v[10:11] op_sel:[1,0,0]
	v_pk_fma_f32 v[12:13], s[72:73], v[70:71], v[12:13] op_sel:[1,0,0]
	v_pk_fma_f32 v[6:7], s[80:81], v[68:69], v[6:7] op_sel:[1,0,0]
	v_pk_fma_f32 v[8:9], s[80:81], v[70:71], v[8:9] op_sel:[1,0,0]
	v_pk_fma_f32 v[2:3], s[88:89], v[68:69], v[2:3] op_sel:[1,0,0]
	v_pk_fma_f32 v[4:5], s[88:89], v[70:71], v[4:5] op_sel:[1,0,0]
	s_waitcnt vmcnt(21)
	v_pk_fma_f32 v[14:15], s[66:67], v[72:73], v[14:15] op_sel_hi:[0,1,1]
	v_pk_fma_f32 v[16:17], s[66:67], v[74:75], v[16:17] op_sel_hi:[0,1,1]
	v_pk_fma_f32 v[10:11], s[74:75], v[72:73], v[10:11] op_sel_hi:[0,1,1]
	v_pk_fma_f32 v[12:13], s[74:75], v[74:75], v[12:13] op_sel_hi:[0,1,1]
	v_pk_fma_f32 v[6:7], s[82:83], v[72:73], v[6:7] op_sel_hi:[0,1,1]
	v_pk_fma_f32 v[8:9], s[82:83], v[74:75], v[8:9] op_sel_hi:[0,1,1]
	v_pk_fma_f32 v[2:3], s[90:91], v[72:73], v[2:3] op_sel_hi:[0,1,1]
	v_pk_fma_f32 v[4:5], s[90:91], v[74:75], v[4:5] op_sel_hi:[0,1,1]
	s_waitcnt vmcnt(20)
	v_pk_fma_f32 v[14:15], s[66:67], v[76:77], v[14:15] op_sel:[1,0,0]
	v_pk_fma_f32 v[16:17], s[66:67], v[78:79], v[16:17] op_sel:[1,0,0]
	v_pk_fma_f32 v[10:11], s[74:75], v[76:77], v[10:11] op_sel:[1,0,0]
	v_pk_fma_f32 v[12:13], s[74:75], v[78:79], v[12:13] op_sel:[1,0,0]
	v_pk_fma_f32 v[6:7], s[82:83], v[76:77], v[6:7] op_sel:[1,0,0]
	v_pk_fma_f32 v[8:9], s[82:83], v[78:79], v[8:9] op_sel:[1,0,0]
	v_pk_fma_f32 v[2:3], s[90:91], v[76:77], v[2:3] op_sel:[1,0,0]
	v_pk_fma_f32 v[4:5], s[90:91], v[78:79], v[4:5] op_sel:[1,0,0]
	s_waitcnt vmcnt(19)
	v_pk_fma_f32 v[14:15], s[68:69], v[80:81], v[14:15] op_sel_hi:[0,1,1]
	v_pk_fma_f32 v[16:17], s[68:69], v[82:83], v[16:17] op_sel_hi:[0,1,1]
	v_pk_fma_f32 v[10:11], s[76:77], v[80:81], v[10:11] op_sel_hi:[0,1,1]
	v_pk_fma_f32 v[12:13], s[76:77], v[82:83], v[12:13] op_sel_hi:[0,1,1]
	v_pk_fma_f32 v[6:7], s[84:85], v[80:81], v[6:7] op_sel_hi:[0,1,1]
	v_pk_fma_f32 v[8:9], s[84:85], v[82:83], v[8:9] op_sel_hi:[0,1,1]
	v_pk_fma_f32 v[2:3], s[92:93], v[80:81], v[2:3] op_sel_hi:[0,1,1]
	v_pk_fma_f32 v[4:5], s[92:93], v[82:83], v[4:5] op_sel_hi:[0,1,1]
	s_waitcnt vmcnt(18)
	v_pk_fma_f32 v[14:15], s[68:69], v[84:85], v[14:15] op_sel:[1,0,0]
	v_pk_fma_f32 v[16:17], s[68:69], v[86:87], v[16:17] op_sel:[1,0,0]
	v_pk_fma_f32 v[10:11], s[76:77], v[84:85], v[10:11] op_sel:[1,0,0]
	v_pk_fma_f32 v[12:13], s[76:77], v[86:87], v[12:13] op_sel:[1,0,0]
	v_pk_fma_f32 v[6:7], s[84:85], v[84:85], v[6:7] op_sel:[1,0,0]
	v_pk_fma_f32 v[8:9], s[84:85], v[86:87], v[8:9] op_sel:[1,0,0]
	v_pk_fma_f32 v[2:3], s[92:93], v[84:85], v[2:3] op_sel:[1,0,0]
	v_pk_fma_f32 v[4:5], s[92:93], v[86:87], v[4:5] op_sel:[1,0,0]
	s_waitcnt vmcnt(17)
	v_pk_fma_f32 v[14:15], s[70:71], v[88:89], v[14:15] op_sel_hi:[0,1,1]
	v_pk_fma_f32 v[16:17], s[70:71], v[90:91], v[16:17] op_sel_hi:[0,1,1]
	v_pk_fma_f32 v[10:11], s[78:79], v[88:89], v[10:11] op_sel_hi:[0,1,1]
	v_pk_fma_f32 v[12:13], s[78:79], v[90:91], v[12:13] op_sel_hi:[0,1,1]
	v_pk_fma_f32 v[6:7], s[86:87], v[88:89], v[6:7] op_sel_hi:[0,1,1]
	v_pk_fma_f32 v[8:9], s[86:87], v[90:91], v[8:9] op_sel_hi:[0,1,1]
	v_pk_fma_f32 v[2:3], s[94:95], v[88:89], v[2:3] op_sel_hi:[0,1,1]
	v_pk_fma_f32 v[4:5], s[94:95], v[90:91], v[4:5] op_sel_hi:[0,1,1]
	s_waitcnt vmcnt(16)
	v_pk_fma_f32 v[14:15], s[70:71], v[92:93], v[14:15] op_sel:[1,0,0]
	v_pk_fma_f32 v[16:17], s[70:71], v[94:95], v[16:17] op_sel:[1,0,0]
	v_pk_fma_f32 v[10:11], s[78:79], v[92:93], v[10:11] op_sel:[1,0,0]
	v_pk_fma_f32 v[12:13], s[78:79], v[94:95], v[12:13] op_sel:[1,0,0]
	v_pk_fma_f32 v[6:7], s[86:87], v[92:93], v[6:7] op_sel:[1,0,0]
	v_pk_fma_f32 v[8:9], s[86:87], v[94:95], v[8:9] op_sel:[1,0,0]
	v_pk_fma_f32 v[2:3], s[94:95], v[92:93], v[2:3] op_sel:[1,0,0]
	v_pk_fma_f32 v[4:5], s[94:95], v[94:95], v[4:5] op_sel:[1,0,0]
	s_waitcnt lgkmcnt(0)
	s_load_dwordx8 s[64:71], s[20:21], 0x60
	s_load_dwordx8 s[72:79], s[20:21], 0x260
	s_load_dwordx8 s[80:87], s[20:21], 0x460
	s_load_dwordx8 s[88:95], s[20:21], 0x660
	s_waitcnt vmcnt(15)
	v_pk_fma_f32 v[14:15], s[32:33], v[96:97], v[14:15] op_sel_hi:[0,1,1]
	v_pk_fma_f32 v[16:17], s[32:33], v[98:99], v[16:17] op_sel_hi:[0,1,1]
	v_pk_fma_f32 v[10:11], s[40:41], v[96:97], v[10:11] op_sel_hi:[0,1,1]
	v_pk_fma_f32 v[12:13], s[40:41], v[98:99], v[12:13] op_sel_hi:[0,1,1]
	v_pk_fma_f32 v[6:7], s[48:49], v[96:97], v[6:7] op_sel_hi:[0,1,1]
	v_pk_fma_f32 v[8:9], s[48:49], v[98:99], v[8:9] op_sel_hi:[0,1,1]
	v_pk_fma_f32 v[2:3], s[56:57], v[96:97], v[2:3] op_sel_hi:[0,1,1]
	v_pk_fma_f32 v[4:5], s[56:57], v[98:99], v[4:5] op_sel_hi:[0,1,1]
	s_waitcnt vmcnt(14)
	v_pk_fma_f32 v[14:15], s[32:33], v[100:101], v[14:15] op_sel:[1,0,0]
	v_pk_fma_f32 v[16:17], s[32:33], v[102:103], v[16:17] op_sel:[1,0,0]
	v_pk_fma_f32 v[10:11], s[40:41], v[100:101], v[10:11] op_sel:[1,0,0]
	v_pk_fma_f32 v[12:13], s[40:41], v[102:103], v[12:13] op_sel:[1,0,0]
	v_pk_fma_f32 v[6:7], s[48:49], v[100:101], v[6:7] op_sel:[1,0,0]
	v_pk_fma_f32 v[8:9], s[48:49], v[102:103], v[8:9] op_sel:[1,0,0]
	v_pk_fma_f32 v[2:3], s[56:57], v[100:101], v[2:3] op_sel:[1,0,0]
	v_pk_fma_f32 v[4:5], s[56:57], v[102:103], v[4:5] op_sel:[1,0,0]
	s_waitcnt vmcnt(13)
	v_pk_fma_f32 v[14:15], s[34:35], v[104:105], v[14:15] op_sel_hi:[0,1,1]
	v_pk_fma_f32 v[16:17], s[34:35], v[106:107], v[16:17] op_sel_hi:[0,1,1]
	v_pk_fma_f32 v[10:11], s[42:43], v[104:105], v[10:11] op_sel_hi:[0,1,1]
	v_pk_fma_f32 v[12:13], s[42:43], v[106:107], v[12:13] op_sel_hi:[0,1,1]
	v_pk_fma_f32 v[6:7], s[50:51], v[104:105], v[6:7] op_sel_hi:[0,1,1]
	v_pk_fma_f32 v[8:9], s[50:51], v[106:107], v[8:9] op_sel_hi:[0,1,1]
	v_pk_fma_f32 v[2:3], s[58:59], v[104:105], v[2:3] op_sel_hi:[0,1,1]
	v_pk_fma_f32 v[4:5], s[58:59], v[106:107], v[4:5] op_sel_hi:[0,1,1]
	s_waitcnt vmcnt(12)
	v_pk_fma_f32 v[14:15], s[34:35], v[108:109], v[14:15] op_sel:[1,0,0]
	v_pk_fma_f32 v[16:17], s[34:35], v[110:111], v[16:17] op_sel:[1,0,0]
	v_pk_fma_f32 v[10:11], s[42:43], v[108:109], v[10:11] op_sel:[1,0,0]
	v_pk_fma_f32 v[12:13], s[42:43], v[110:111], v[12:13] op_sel:[1,0,0]
	v_pk_fma_f32 v[6:7], s[50:51], v[108:109], v[6:7] op_sel:[1,0,0]
	v_pk_fma_f32 v[8:9], s[50:51], v[110:111], v[8:9] op_sel:[1,0,0]
	v_pk_fma_f32 v[2:3], s[58:59], v[108:109], v[2:3] op_sel:[1,0,0]
	v_pk_fma_f32 v[4:5], s[58:59], v[110:111], v[4:5] op_sel:[1,0,0]
	s_waitcnt vmcnt(11)
	v_pk_fma_f32 v[14:15], s[36:37], v[112:113], v[14:15] op_sel_hi:[0,1,1]
	v_pk_fma_f32 v[16:17], s[36:37], v[114:115], v[16:17] op_sel_hi:[0,1,1]
	v_pk_fma_f32 v[10:11], s[44:45], v[112:113], v[10:11] op_sel_hi:[0,1,1]
	v_pk_fma_f32 v[12:13], s[44:45], v[114:115], v[12:13] op_sel_hi:[0,1,1]
	v_pk_fma_f32 v[6:7], s[52:53], v[112:113], v[6:7] op_sel_hi:[0,1,1]
	v_pk_fma_f32 v[8:9], s[52:53], v[114:115], v[8:9] op_sel_hi:[0,1,1]
	v_pk_fma_f32 v[2:3], s[60:61], v[112:113], v[2:3] op_sel_hi:[0,1,1]
	v_pk_fma_f32 v[4:5], s[60:61], v[114:115], v[4:5] op_sel_hi:[0,1,1]
	s_waitcnt vmcnt(10)
	v_pk_fma_f32 v[14:15], s[36:37], v[116:117], v[14:15] op_sel:[1,0,0]
	v_pk_fma_f32 v[16:17], s[36:37], v[118:119], v[16:17] op_sel:[1,0,0]
	v_pk_fma_f32 v[10:11], s[44:45], v[116:117], v[10:11] op_sel:[1,0,0]
	v_pk_fma_f32 v[12:13], s[44:45], v[118:119], v[12:13] op_sel:[1,0,0]
	v_pk_fma_f32 v[6:7], s[52:53], v[116:117], v[6:7] op_sel:[1,0,0]
	v_pk_fma_f32 v[8:9], s[52:53], v[118:119], v[8:9] op_sel:[1,0,0]
	v_pk_fma_f32 v[2:3], s[60:61], v[116:117], v[2:3] op_sel:[1,0,0]
	v_pk_fma_f32 v[4:5], s[60:61], v[118:119], v[4:5] op_sel:[1,0,0]
	s_waitcnt vmcnt(9)
	v_pk_fma_f32 v[14:15], s[38:39], v[120:121], v[14:15] op_sel_hi:[0,1,1]
	v_pk_fma_f32 v[16:17], s[38:39], v[122:123], v[16:17] op_sel_hi:[0,1,1]
	v_pk_fma_f32 v[10:11], s[46:47], v[120:121], v[10:11] op_sel_hi:[0,1,1]
	v_pk_fma_f32 v[12:13], s[46:47], v[122:123], v[12:13] op_sel_hi:[0,1,1]
	v_pk_fma_f32 v[6:7], s[54:55], v[120:121], v[6:7] op_sel_hi:[0,1,1]
	v_pk_fma_f32 v[8:9], s[54:55], v[122:123], v[8:9] op_sel_hi:[0,1,1]
	v_pk_fma_f32 v[2:3], s[62:63], v[120:121], v[2:3] op_sel_hi:[0,1,1]
	v_pk_fma_f32 v[4:5], s[62:63], v[122:123], v[4:5] op_sel_hi:[0,1,1]
	s_waitcnt vmcnt(8)
	v_pk_fma_f32 v[14:15], s[38:39], v[124:125], v[14:15] op_sel:[1,0,0]
	v_pk_fma_f32 v[16:17], s[38:39], v[126:127], v[16:17] op_sel:[1,0,0]
	v_pk_fma_f32 v[10:11], s[46:47], v[124:125], v[10:11] op_sel:[1,0,0]
	v_pk_fma_f32 v[12:13], s[46:47], v[126:127], v[12:13] op_sel:[1,0,0]
	v_pk_fma_f32 v[6:7], s[54:55], v[124:125], v[6:7] op_sel:[1,0,0]
	v_pk_fma_f32 v[8:9], s[54:55], v[126:127], v[8:9] op_sel:[1,0,0]
	v_pk_fma_f32 v[2:3], s[62:63], v[124:125], v[2:3] op_sel:[1,0,0]
	v_pk_fma_f32 v[4:5], s[62:63], v[126:127], v[4:5] op_sel:[1,0,0]
	s_waitcnt lgkmcnt(0)
	s_waitcnt vmcnt(7)
	v_pk_fma_f32 v[14:15], s[64:65], v[128:129], v[14:15] op_sel_hi:[0,1,1]
	v_pk_fma_f32 v[16:17], s[64:65], v[130:131], v[16:17] op_sel_hi:[0,1,1]
	v_pk_fma_f32 v[10:11], s[72:73], v[128:129], v[10:11] op_sel_hi:[0,1,1]
	v_pk_fma_f32 v[12:13], s[72:73], v[130:131], v[12:13] op_sel_hi:[0,1,1]
	v_pk_fma_f32 v[6:7], s[80:81], v[128:129], v[6:7] op_sel_hi:[0,1,1]
	v_pk_fma_f32 v[8:9], s[80:81], v[130:131], v[8:9] op_sel_hi:[0,1,1]
	v_pk_fma_f32 v[2:3], s[88:89], v[128:129], v[2:3] op_sel_hi:[0,1,1]
	v_pk_fma_f32 v[4:5], s[88:89], v[130:131], v[4:5] op_sel_hi:[0,1,1]
	s_waitcnt vmcnt(6)
	v_pk_fma_f32 v[14:15], s[64:65], v[132:133], v[14:15] op_sel:[1,0,0]
	v_pk_fma_f32 v[16:17], s[64:65], v[134:135], v[16:17] op_sel:[1,0,0]
	v_pk_fma_f32 v[10:11], s[72:73], v[132:133], v[10:11] op_sel:[1,0,0]
	v_pk_fma_f32 v[12:13], s[72:73], v[134:135], v[12:13] op_sel:[1,0,0]
	v_pk_fma_f32 v[6:7], s[80:81], v[132:133], v[6:7] op_sel:[1,0,0]
	v_pk_fma_f32 v[8:9], s[80:81], v[134:135], v[8:9] op_sel:[1,0,0]
	v_pk_fma_f32 v[2:3], s[88:89], v[132:133], v[2:3] op_sel:[1,0,0]
	v_pk_fma_f32 v[4:5], s[88:89], v[134:135], v[4:5] op_sel:[1,0,0]
	s_waitcnt vmcnt(5)
	v_pk_fma_f32 v[14:15], s[66:67], v[136:137], v[14:15] op_sel_hi:[0,1,1]
	v_pk_fma_f32 v[16:17], s[66:67], v[138:139], v[16:17] op_sel_hi:[0,1,1]
	v_pk_fma_f32 v[10:11], s[74:75], v[136:137], v[10:11] op_sel_hi:[0,1,1]
	v_pk_fma_f32 v[12:13], s[74:75], v[138:139], v[12:13] op_sel_hi:[0,1,1]
	v_pk_fma_f32 v[6:7], s[82:83], v[136:137], v[6:7] op_sel_hi:[0,1,1]
	v_pk_fma_f32 v[8:9], s[82:83], v[138:139], v[8:9] op_sel_hi:[0,1,1]
	v_pk_fma_f32 v[2:3], s[90:91], v[136:137], v[2:3] op_sel_hi:[0,1,1]
	v_pk_fma_f32 v[4:5], s[90:91], v[138:139], v[4:5] op_sel_hi:[0,1,1]
	s_waitcnt vmcnt(4)
	v_pk_fma_f32 v[14:15], s[66:67], v[140:141], v[14:15] op_sel:[1,0,0]
	v_pk_fma_f32 v[16:17], s[66:67], v[142:143], v[16:17] op_sel:[1,0,0]
	v_pk_fma_f32 v[10:11], s[74:75], v[140:141], v[10:11] op_sel:[1,0,0]
	v_pk_fma_f32 v[12:13], s[74:75], v[142:143], v[12:13] op_sel:[1,0,0]
	v_pk_fma_f32 v[6:7], s[82:83], v[140:141], v[6:7] op_sel:[1,0,0]
	v_pk_fma_f32 v[8:9], s[82:83], v[142:143], v[8:9] op_sel:[1,0,0]
	v_pk_fma_f32 v[2:3], s[90:91], v[140:141], v[2:3] op_sel:[1,0,0]
	v_pk_fma_f32 v[4:5], s[90:91], v[142:143], v[4:5] op_sel:[1,0,0]
	s_waitcnt vmcnt(3)
	v_pk_fma_f32 v[14:15], s[68:69], v[144:145], v[14:15] op_sel_hi:[0,1,1]
	v_pk_fma_f32 v[16:17], s[68:69], v[146:147], v[16:17] op_sel_hi:[0,1,1]
	v_pk_fma_f32 v[10:11], s[76:77], v[144:145], v[10:11] op_sel_hi:[0,1,1]
	v_pk_fma_f32 v[12:13], s[76:77], v[146:147], v[12:13] op_sel_hi:[0,1,1]
	v_pk_fma_f32 v[6:7], s[84:85], v[144:145], v[6:7] op_sel_hi:[0,1,1]
	v_pk_fma_f32 v[8:9], s[84:85], v[146:147], v[8:9] op_sel_hi:[0,1,1]
	v_pk_fma_f32 v[2:3], s[92:93], v[144:145], v[2:3] op_sel_hi:[0,1,1]
	v_pk_fma_f32 v[4:5], s[92:93], v[146:147], v[4:5] op_sel_hi:[0,1,1]
	s_waitcnt vmcnt(2)
	v_pk_fma_f32 v[14:15], s[68:69], v[148:149], v[14:15] op_sel:[1,0,0]
	v_pk_fma_f32 v[16:17], s[68:69], v[150:151], v[16:17] op_sel:[1,0,0]
	v_pk_fma_f32 v[10:11], s[76:77], v[148:149], v[10:11] op_sel:[1,0,0]
	v_pk_fma_f32 v[12:13], s[76:77], v[150:151], v[12:13] op_sel:[1,0,0]
	v_pk_fma_f32 v[6:7], s[84:85], v[148:149], v[6:7] op_sel:[1,0,0]
	v_pk_fma_f32 v[8:9], s[84:85], v[150:151], v[8:9] op_sel:[1,0,0]
	v_pk_fma_f32 v[2:3], s[92:93], v[148:149], v[2:3] op_sel:[1,0,0]
	v_pk_fma_f32 v[4:5], s[92:93], v[150:151], v[4:5] op_sel:[1,0,0]
	s_waitcnt vmcnt(1)
	v_pk_fma_f32 v[14:15], s[70:71], v[152:153], v[14:15] op_sel_hi:[0,1,1]
	v_pk_fma_f32 v[16:17], s[70:71], v[154:155], v[16:17] op_sel_hi:[0,1,1]
	v_pk_fma_f32 v[10:11], s[78:79], v[152:153], v[10:11] op_sel_hi:[0,1,1]
	v_pk_fma_f32 v[12:13], s[78:79], v[154:155], v[12:13] op_sel_hi:[0,1,1]
	v_pk_fma_f32 v[6:7], s[86:87], v[152:153], v[6:7] op_sel_hi:[0,1,1]
	v_pk_fma_f32 v[8:9], s[86:87], v[154:155], v[8:9] op_sel_hi:[0,1,1]
	v_pk_fma_f32 v[2:3], s[94:95], v[152:153], v[2:3] op_sel_hi:[0,1,1]
	v_pk_fma_f32 v[4:5], s[94:95], v[154:155], v[4:5] op_sel_hi:[0,1,1]
	s_waitcnt vmcnt(0)
	v_pk_fma_f32 v[14:15], s[70:71], v[156:157], v[14:15] op_sel:[1,0,0]
	v_pk_fma_f32 v[16:17], s[70:71], v[158:159], v[16:17] op_sel:[1,0,0]
	v_pk_fma_f32 v[10:11], s[78:79], v[156:157], v[10:11] op_sel:[1,0,0]
	v_pk_fma_f32 v[12:13], s[78:79], v[158:159], v[12:13] op_sel:[1,0,0]
	v_pk_fma_f32 v[6:7], s[86:87], v[156:157], v[6:7] op_sel:[1,0,0]
	v_pk_fma_f32 v[8:9], s[86:87], v[158:159], v[8:9] op_sel:[1,0,0]
	v_pk_fma_f32 v[2:3], s[94:95], v[156:157], v[2:3] op_sel:[1,0,0]
	v_pk_fma_f32 v[4:5], s[94:95], v[158:159], v[4:5] op_sel:[1,0,0]
	s_lshl_b32 s9, s26, 12
	v_add_u32_e32 v18, s9, v26
	s_cmp_eq_u32 s22, 0
	s_cbranch_scc1 .Lprep_a0_wait
	s_sub_u32 s8, s22, 1
	s_lshl_b32 s8, s8, 13
	v_add_u32_e32 v19, s8, v18
	ds_write_b128 v19, v[14:17] offset:0
	ds_write_b128 v19, v[10:13] offset:1024
	ds_write_b128 v19, v[6:9] offset:2048
	ds_write_b128 v19, v[2:5] offset:3072
.Lprep_a0_wait:
	s_waitcnt lgkmcnt(0)
	s_barrier
	s_cmp_lg_u32 s22, 0
	s_cbranch_scc1 .LBB0_7
	ds_read_b128 v[32:35], v18 offset:0
	ds_read_b128 v[36:39], v18 offset:8192
	ds_read_b128 v[40:43], v18 offset:16384
	ds_read_b128 v[44:47], v18 offset:1024
	ds_read_b128 v[48:51], v18 offset:9216
	ds_read_b128 v[52:55], v18 offset:17408
	ds_read_b128 v[56:59], v18 offset:2048
	ds_read_b128 v[60:63], v18 offset:10240
	ds_read_b128 v[64:67], v18 offset:18432
	ds_read_b128 v[68:71], v18 offset:3072
	ds_read_b128 v[72:75], v18 offset:11264
	ds_read_b128 v[76:79], v18 offset:19456
	s_lshl_b32 s8, s31, 11
	s_lshl_b32 s9, s30, 10
	s_add_u32 s8, s8, s9
	s_add_u32 s28, s28, s8
	s_addc_u32 s29, s29, 0
	s_waitcnt lgkmcnt(11)
	v_pk_add_f32 v[14:15], v[14:15], v[32:33]
	v_pk_add_f32 v[16:17], v[16:17], v[34:35]
	s_waitcnt lgkmcnt(10)
	v_pk_add_f32 v[14:15], v[14:15], v[36:37]
	v_pk_add_f32 v[16:17], v[16:17], v[38:39]
	s_waitcnt lgkmcnt(9)
	v_pk_add_f32 v[14:15], v[14:15], v[40:41]
	v_pk_add_f32 v[16:17], v[16:17], v[42:43]
	global_store_dwordx4 v26, v[14:17], s[28:29]
	s_waitcnt lgkmcnt(8)
	v_pk_add_f32 v[10:11], v[10:11], v[44:45]
	v_pk_add_f32 v[12:13], v[12:13], v[46:47]
	s_waitcnt lgkmcnt(7)
	v_pk_add_f32 v[10:11], v[10:11], v[48:49]
	v_pk_add_f32 v[12:13], v[12:13], v[50:51]
	s_waitcnt lgkmcnt(6)
	v_pk_add_f32 v[10:11], v[10:11], v[52:53]
	v_pk_add_f32 v[12:13], v[12:13], v[54:55]
	global_store_dwordx4 v26, v[10:13], s[28:29] offset:2048
	s_waitcnt lgkmcnt(5)
	v_pk_add_f32 v[6:7], v[6:7], v[56:57]
	v_pk_add_f32 v[8:9], v[8:9], v[58:59]
	s_waitcnt lgkmcnt(4)
	v_pk_add_f32 v[6:7], v[6:7], v[60:61]
	v_pk_add_f32 v[8:9], v[8:9], v[62:63]
	s_waitcnt lgkmcnt(3)
	v_pk_add_f32 v[6:7], v[6:7], v[64:65]
	v_pk_add_f32 v[8:9], v[8:9], v[66:67]
	s_add_u32 s28, s28, 0x1000
	s_addc_u32 s29, s29, 0
	global_store_dwordx4 v26, v[6:9], s[28:29]
	s_waitcnt lgkmcnt(2)
	v_pk_add_f32 v[2:3], v[2:3], v[68:69]
	v_pk_add_f32 v[4:5], v[4:5], v[70:71]
	s_waitcnt lgkmcnt(1)
	v_pk_add_f32 v[2:3], v[2:3], v[72:73]
	v_pk_add_f32 v[4:5], v[4:5], v[74:75]
	s_waitcnt lgkmcnt(0)
	v_pk_add_f32 v[2:3], v[2:3], v[76:77]
	v_pk_add_f32 v[4:5], v[4:5], v[78:79]
	global_store_dwordx4 v26, v[2:5], s[28:29] offset:2048
